# speedup vs baseline: 1.0152x; 1.0152x over previous
_Z9ssim_mainPKfS0_S0_Pf:
	v_readfirstlane_b32 s29, v0
	v_cmp_gt_u32_e32 vcc, 32, v0
	s_nop 1
	s_and_saveexec_b64 s[30:31], vcc
	v_mov_b32_e32 v1, 0x10000
	v_lshl_or_b32 v1, v0, 2, v1
	v_mov_b32_e32 v2, 0
	ds_write_b32 v1, v2
	s_or_b64 exec, exec, s[30:31]
	s_load_dwordx4 s[4:7], s[0:1], 0x0
	s_load_dwordx4 s[8:11], s[0:1], 0x10
	s_lshr_b32 s12, s29, 6
	s_mov_b32 s51, 0x44800000
	s_mov_b32 s38, 0
	s_mov_b32 s39, -1
	s_mov_b32 s92, -1
	s_mov_b32 s93, 0xffff
	s_mov_b32 s94, 0xffff
	s_mov_b32 s95, 0xffff
	v_and_b32_e32 v8, 63, v0
	v_and_b32_e32 v169, 15, v0
	v_bfe_u32 v164, v0, 4, 2
	v_lshlrev_b32_e32 v167, 3, v164
	v_xor_b32_e32 v168, 16, v167
	v_sub_u32_e32 v165, v167, v169
	v_sub_u32_e32 v166, v168, v169
	v_add_u32_e32 v172, 0, v165
	v_med3_i32 v172, v172, 0, 10
	v_lshlrev_b32_e32 v172, 2, v172
	v_add_u32_e32 v173, 1, v165
	v_med3_i32 v173, v173, 0, 10
	v_lshlrev_b32_e32 v173, 2, v173
	v_add_u32_e32 v174, 2, v165
	v_med3_i32 v174, v174, 0, 10
	v_lshlrev_b32_e32 v174, 2, v174
	v_add_u32_e32 v175, 3, v165
	v_med3_i32 v175, v175, 0, 10
	v_lshlrev_b32_e32 v175, 2, v175
	v_add_u32_e32 v176, 4, v165
	v_med3_i32 v176, v176, 0, 10
	v_lshlrev_b32_e32 v176, 2, v176
	v_add_u32_e32 v177, 5, v165
	v_med3_i32 v177, v177, 0, 10
	v_lshlrev_b32_e32 v177, 2, v177
	v_add_u32_e32 v178, 6, v165
	v_med3_i32 v178, v178, 0, 10
	v_lshlrev_b32_e32 v178, 2, v178
	v_add_u32_e32 v179, 7, v165
	v_med3_i32 v179, v179, 0, 10
	v_lshlrev_b32_e32 v179, 2, v179
	v_add_u32_e32 v180, 0, v166
	v_med3_i32 v180, v180, 0, 10
	v_lshlrev_b32_e32 v180, 2, v180
	v_add_u32_e32 v181, 1, v166
	v_med3_i32 v181, v181, 0, 10
	v_lshlrev_b32_e32 v181, 2, v181
	v_add_u32_e32 v182, 2, v166
	v_med3_i32 v182, v182, 0, 10
	v_lshlrev_b32_e32 v182, 2, v182
	v_add_u32_e32 v183, 3, v166
	v_med3_i32 v183, v183, 0, 10
	v_lshlrev_b32_e32 v183, 2, v183
	v_add_u32_e32 v184, 4, v166
	v_med3_i32 v184, v184, 0, 10
	v_lshlrev_b32_e32 v184, 2, v184
	v_add_u32_e32 v185, 5, v166
	v_med3_i32 v185, v185, 0, 10
	v_lshlrev_b32_e32 v185, 2, v185
	v_add_u32_e32 v186, 6, v166
	v_med3_i32 v186, v186, 0, 10
	v_lshlrev_b32_e32 v186, 2, v186
	v_add_u32_e32 v187, 7, v166
	v_med3_i32 v187, v187, 0, 10
	v_lshlrev_b32_e32 v187, 2, v187
	s_waitcnt lgkmcnt(0)
	global_load_dword v188, v172, s[8:9]
	global_load_dword v189, v173, s[8:9]
	global_load_dword v190, v174, s[8:9]
	global_load_dword v191, v175, s[8:9]
	global_load_dword v192, v176, s[8:9]
	global_load_dword v193, v177, s[8:9]
	global_load_dword v194, v178, s[8:9]
	global_load_dword v195, v179, s[8:9]
	global_load_dword v196, v180, s[8:9]
	global_load_dword v197, v181, s[8:9]
	global_load_dword v198, v182, s[8:9]
	global_load_dword v199, v183, s[8:9]
	global_load_dword v200, v184, s[8:9]
	global_load_dword v201, v185, s[8:9]
	global_load_dword v202, v186, s[8:9]
	global_load_dword v203, v187, s[8:9]
	s_load_dwordx8 s[40:47], s[8:9], 0x0
	s_load_dwordx2 s[48:49], s[8:9], 0x20
	s_load_dword s50, s[8:9], 0x28
	s_and_b32 s13, s2, 7
	s_lshl_b32 s13, s13, 5
	s_lshr_b32 s14, s2, 3
	s_add_u32 s13, s13, s14
	s_lshr_b32 s14, s13, 3
	s_and_b32 s15, s13, 7
	s_lshl_b32 s16, s14, 20
	s_lshl_b32 s17, s15, 17
	s_add_u32 s16, s16, s17
	s_lshl_b32 s17, s12, 8
	s_add_u32 s16, s16, s17
	s_add_u32 s18, s4, s16
	s_addc_u32 s19, s5, 0
	s_add_u32 s20, s6, s16
	s_addc_u32 s21, s7, 0
	s_mov_b32 s52, s18
	s_mov_b32 s53, s19
	s_add_u32 s54, s18, 0x1000
	s_addc_u32 s55, s19, 0
	s_add_u32 s56, s18, 0x2000
	s_addc_u32 s57, s19, 0
	s_add_u32 s58, s18, 0x3000
	s_addc_u32 s59, s19, 0
	s_add_u32 s60, s18, 0x10000
	s_addc_u32 s61, s19, 0
	s_add_u32 s62, s18, 0x11000
	s_addc_u32 s63, s19, 0
	s_add_u32 s64, s18, 0x12000
	s_addc_u32 s65, s19, 0
	s_add_u32 s66, s18, 0x13000
	s_addc_u32 s67, s19, 0
	s_mov_b32 s68, s20
	s_mov_b32 s69, s21
	s_add_u32 s70, s20, 0x1000
	s_addc_u32 s71, s21, 0
	s_add_u32 s72, s20, 0x2000
	s_addc_u32 s73, s21, 0
	s_add_u32 s74, s20, 0x3000
	s_addc_u32 s75, s21, 0
	s_add_u32 s76, s20, 0x10000
	s_addc_u32 s77, s21, 0
	s_add_u32 s78, s20, 0x11000
	s_addc_u32 s79, s21, 0
	s_add_u32 s80, s20, 0x12000
	s_addc_u32 s81, s21, 0
	s_add_u32 s82, s20, 0x13000
	s_addc_u32 s83, s21, 0
	s_cmp_eq_u32 s15, 7
	s_cselect_b32 s22, 0, 0x20000
	s_add_u32 s84, s18, s22
	s_addc_u32 s85, s19, 0
	s_add_u32 s86, s18, s22
	s_addc_u32 s87, s19, 0
	s_add_u32 s86, s86, 0x1000
	s_addc_u32 s87, s87, 0
	s_add_u32 s88, s20, s22
	s_addc_u32 s89, s21, 0
	s_add_u32 s90, s20, s22
	s_addc_u32 s91, s21, 0
	s_add_u32 s90, s90, 0x1000
	s_addc_u32 s91, s91, 0
	v_lshrrev_b32_e32 v167, 2, v169
	v_lshlrev_b32_e32 v167, 5, v167
	v_and_b32_e32 v168, 1, v169
	v_lshl_or_b32 v167, v168, 4, v167
	v_bfe_u32 v168, v169, 1, 1
	v_lshl_or_b32 v167, v168, 7, v167
	v_lshl_or_b32 v9, v164, 14, v167
	v_and_b32_e32 v168, 1, v164
	v_lshl_or_b32 v23, v168, 14, v167
	v_lshrrev_b32_e32 v168, 1, v164
	v_lshl_or_b32 v23, v168, 13, v23
	global_load_dwordx4 v[36:39], v9, s[52:53] offset:0 sc1 nt
	global_load_dwordx4 v[40:43], v9, s[52:53] offset:2048 sc1 nt
	global_load_dwordx4 v[68:71], v9, s[68:69] offset:0 sc1 nt
	global_load_dwordx4 v[72:75], v9, s[68:69] offset:2048 sc1 nt
	global_load_dwordx4 v[44:47], v9, s[54:55] offset:0 sc1 nt
	global_load_dwordx4 v[48:51], v9, s[54:55] offset:2048 sc1 nt
	global_load_dwordx4 v[76:79], v9, s[70:71] offset:0 sc1 nt
	global_load_dwordx4 v[80:83], v9, s[70:71] offset:2048 sc1 nt
	global_load_dwordx4 v[52:55], v9, s[56:57] offset:0 sc1 nt
	global_load_dwordx4 v[56:59], v9, s[56:57] offset:2048 sc1 nt
	global_load_dwordx4 v[84:87], v9, s[72:73] offset:0 sc1 nt
	global_load_dwordx4 v[88:91], v9, s[72:73] offset:2048 sc1 nt
	global_load_dwordx4 v[60:63], v9, s[58:59] offset:0 sc1 nt
	global_load_dwordx4 v[64:67], v9, s[58:59] offset:2048 sc1 nt
	global_load_dwordx4 v[92:95], v9, s[74:75] offset:0 sc1 nt
	global_load_dwordx4 v[96:99], v9, s[74:75] offset:2048 sc1 nt
	global_load_dwordx4 v[100:103], v9, s[60:61] offset:0 sc1 nt
	global_load_dwordx4 v[104:107], v9, s[60:61] offset:2048 sc1 nt
	global_load_dwordx4 v[132:135], v9, s[76:77] offset:0 sc1 nt
	global_load_dwordx4 v[136:139], v9, s[76:77] offset:2048 sc1 nt
	global_load_dwordx4 v[108:111], v9, s[62:63] offset:0 sc1 nt
	global_load_dwordx4 v[112:115], v9, s[62:63] offset:2048 sc1 nt
	global_load_dwordx4 v[140:143], v9, s[78:79] offset:0 sc1 nt
	global_load_dwordx4 v[144:147], v9, s[78:79] offset:2048 sc1 nt
	global_load_dwordx4 v[116:119], v9, s[64:65] offset:0 sc1 nt
	global_load_dwordx4 v[120:123], v9, s[64:65] offset:2048 sc1 nt
	global_load_dwordx4 v[148:151], v9, s[80:81] offset:0 sc1 nt
	global_load_dwordx4 v[152:155], v9, s[80:81] offset:2048 sc1 nt
	global_load_dwordx4 v[124:127], v9, s[66:67] offset:0 sc1 nt
	global_load_dwordx4 v[128:131], v9, s[66:67] offset:2048 sc1 nt
	global_load_dwordx4 v[156:159], v9, s[82:83] offset:0 sc1 nt
	global_load_dwordx4 v[160:163], v9, s[82:83] offset:2048 sc1 nt
	s_waitcnt lgkmcnt(0)
	v_mov_b32_e32 v229, 0x44800000
	v_fma_mixlo_f16 v228, s40, v229, 0
	v_cvt_f32_f16_e32 v228, v228
	v_cvt_f64_f32_e32 v[212:213], v228
	v_add_f64 v[212:213], v[212:213], 0
	v_fma_mixlo_f16 v228, s41, v229, 0
	v_cvt_f32_f16_e32 v228, v228
	v_cvt_f64_f32_e32 v[214:215], v228
	v_add_f64 v[212:213], v[212:213], v[214:215]
	v_fma_mixlo_f16 v228, s42, v229, 0
	v_cvt_f32_f16_e32 v228, v228
	v_cvt_f64_f32_e32 v[214:215], v228
	v_add_f64 v[212:213], v[212:213], v[214:215]
	v_fma_mixlo_f16 v228, s43, v229, 0
	v_cvt_f32_f16_e32 v228, v228
	v_cvt_f64_f32_e32 v[214:215], v228
	v_add_f64 v[212:213], v[212:213], v[214:215]
	v_fma_mixlo_f16 v228, s44, v229, 0
	v_cvt_f32_f16_e32 v228, v228
	v_cvt_f64_f32_e32 v[214:215], v228
	v_add_f64 v[212:213], v[212:213], v[214:215]
	v_fma_mixlo_f16 v228, s45, v229, 0
	v_cvt_f32_f16_e32 v228, v228
	v_cvt_f64_f32_e32 v[214:215], v228
	v_add_f64 v[212:213], v[212:213], v[214:215]
	v_fma_mixlo_f16 v228, s46, v229, 0
	v_cvt_f32_f16_e32 v228, v228
	v_cvt_f64_f32_e32 v[214:215], v228
	v_add_f64 v[212:213], v[212:213], v[214:215]
	v_fma_mixlo_f16 v228, s47, v229, 0
	v_cvt_f32_f16_e32 v228, v228
	v_cvt_f64_f32_e32 v[214:215], v228
	v_add_f64 v[212:213], v[212:213], v[214:215]
	v_fma_mixlo_f16 v228, s48, v229, 0
	v_cvt_f32_f16_e32 v228, v228
	v_cvt_f64_f32_e32 v[214:215], v228
	v_add_f64 v[212:213], v[212:213], v[214:215]
	v_fma_mixlo_f16 v228, s49, v229, 0
	v_cvt_f32_f16_e32 v228, v228
	v_cvt_f64_f32_e32 v[214:215], v228
	v_add_f64 v[212:213], v[212:213], v[214:215]
	v_fma_mixlo_f16 v228, s50, v229, 0
	v_cvt_f32_f16_e32 v228, v228
	v_cvt_f64_f32_e32 v[214:215], v228
	v_add_f64 v[212:213], v[212:213], v[214:215]
	v_mul_f64 v[212:213], v[212:213], v[212:213]
	v_mul_f64 v[216:217], v[212:213], 0.5
	v_add_f64 v[218:219], v[216:217], v[216:217]
	s_mov_b32 s36, 0xeb1c432d
	s_mov_b32 s37, 0x3f1a36e2
	v_mul_f64 v[220:221], v[212:213], s[36:37]
	v_mul_f64 v[222:223], v[216:217], v[218:219]
	v_fmac_f64_e32 v[222:223], v[212:213], v[220:221]
	v_add_f64 v[224:225], v[212:213], v[212:213]
	s_mov_b32 s36, 0x487fcb92
	s_mov_b32 s37, 0x3f4d7dbf
	v_mul_f64 v[226:227], v[212:213], s[36:37]
	v_cvt_f32_f64_e32 v0, v[226:227]
	v_mov_b32_e32 v1, v0
	v_mov_b32_e32 v2, v0
	v_mov_b32_e32 v3, v0
	v_cvt_f32_f64_e32 v10, v[218:219]
	v_cvt_f32_f64_e32 v11, v[222:223]
	v_cvt_f32_f64_e32 v12, v[212:213]
	v_cvt_f32_f64_e32 v13, v[224:225]
	v_mul_f64 v[226:227], v[212:213], v[226:227]
	v_cvt_f32_f64_e32 v14, v[226:227]
	v_lshlrev_b32_e32 v167, 2, v164
	s_cmp_eq_u32 s12, 0
	s_cselect_b32 s23, 6, 64
	v_add_u32_e32 v168, 0, v167
	v_cmp_gt_u32_e32 vcc, s23, v168
	s_nop 1
	v_cndmask_b32_e64 v15, 0, 1.0, vcc
	v_add_u32_e32 v168, 1, v167
	v_cmp_gt_u32_e32 vcc, s23, v168
	s_nop 1
	v_cndmask_b32_e64 v16, 0, 1.0, vcc
	v_add_u32_e32 v168, 2, v167
	v_cmp_gt_u32_e32 vcc, s23, v168
	s_nop 1
	v_cndmask_b32_e64 v17, 0, 1.0, vcc
	v_add_u32_e32 v168, 3, v167
	v_cmp_gt_u32_e32 vcc, s23, v168
	s_nop 1
	v_cndmask_b32_e64 v18, 0, 1.0, vcc
	v_and_b32_e32 v167, 31, v8
	v_lshlrev_b32_e32 v167, 4, v167
	s_lshl_b32 s24, s12, 11
	s_add_i32 s25, s12, 7
	s_and_b32 s25, s25, 7
	s_lshl_b32 s26, s25, 11
	v_or_b32_e32 v4, s24, v167
	v_or_b32_e32 v5, s26, v167
	s_lshl_b32 s27, s12, 2
	s_add_u32 s27, s27, 0x10000
	s_lshl_b32 s28, s25, 2
	s_add_u32 s28, s28, 0x10000
	v_mov_b32_e32 v6, s27
	v_mov_b32_e32 v7, s28
	v_mov_b32_e32 v19, 0
	v_mov_b32_e32 v20, 0
	v_mov_b32_e32 v21, 0
	v_mov_b32_e32 v22, 0
	s_waitcnt vmcnt(32)
	v_cmp_lt_u32_e64 s[32:33], 31, v8
	v_cmp_gt_u32_e64 s[34:35], 32, v8
	v_fma_mixlo_f16 v204, v188, s51, 0
	v_add_u32_e32 v167, 0, v165
	v_cmp_gt_u32_e32 vcc, 11, v167
	s_nop 1
	v_cndmask_b32_e32 v204, 0, v204, vcc
	v_fma_mixlo_f16 v205, v189, s51, 0
	v_add_u32_e32 v167, 1, v165
	v_cmp_gt_u32_e32 vcc, 11, v167
	s_nop 1
	v_cndmask_b32_e32 v205, 0, v205, vcc
	v_fma_mixlo_f16 v206, v190, s51, 0
	v_add_u32_e32 v167, 2, v165
	v_cmp_gt_u32_e32 vcc, 11, v167
	s_nop 1
	v_cndmask_b32_e32 v206, 0, v206, vcc
	v_fma_mixlo_f16 v207, v191, s51, 0
	v_add_u32_e32 v167, 3, v165
	v_cmp_gt_u32_e32 vcc, 11, v167
	s_nop 1
	v_cndmask_b32_e32 v207, 0, v207, vcc
	v_fma_mixlo_f16 v208, v192, s51, 0
	v_add_u32_e32 v167, 4, v165
	v_cmp_gt_u32_e32 vcc, 11, v167
	s_nop 1
	v_cndmask_b32_e32 v208, 0, v208, vcc
	v_fma_mixlo_f16 v209, v193, s51, 0
	v_add_u32_e32 v167, 5, v165
	v_cmp_gt_u32_e32 vcc, 11, v167
	s_nop 1
	v_cndmask_b32_e32 v209, 0, v209, vcc
	v_fma_mixlo_f16 v210, v194, s51, 0
	v_add_u32_e32 v167, 6, v165
	v_cmp_gt_u32_e32 vcc, 11, v167
	s_nop 1
	v_cndmask_b32_e32 v210, 0, v210, vcc
	v_fma_mixlo_f16 v211, v195, s51, 0
	v_add_u32_e32 v167, 7, v165
	v_cmp_gt_u32_e32 vcc, 11, v167
	s_nop 1
	v_cndmask_b32_e32 v211, 0, v211, vcc
	v_pack_b32_f16 v24, v204, v205
	v_pack_b32_f16 v25, v206, v207
	v_pack_b32_f16 v26, v208, v209
	v_pack_b32_f16 v27, v210, v211
	v_fma_mixlo_f16 v204, v196, s51, 0
	v_add_u32_e32 v167, 0, v166
	v_cmp_gt_u32_e32 vcc, 11, v167
	s_nop 1
	v_cndmask_b32_e32 v204, 0, v204, vcc
	v_fma_mixlo_f16 v205, v197, s51, 0
	v_add_u32_e32 v167, 1, v166
	v_cmp_gt_u32_e32 vcc, 11, v167
	s_nop 1
	v_cndmask_b32_e32 v205, 0, v205, vcc
	v_fma_mixlo_f16 v206, v198, s51, 0
	v_add_u32_e32 v167, 2, v166
	v_cmp_gt_u32_e32 vcc, 11, v167
	s_nop 1
	v_cndmask_b32_e32 v206, 0, v206, vcc
	v_fma_mixlo_f16 v207, v199, s51, 0
	v_add_u32_e32 v167, 3, v166
	v_cmp_gt_u32_e32 vcc, 11, v167
	s_nop 1
	v_cndmask_b32_e32 v207, 0, v207, vcc
	v_fma_mixlo_f16 v208, v200, s51, 0
	v_add_u32_e32 v167, 4, v166
	v_cmp_gt_u32_e32 vcc, 11, v167
	s_nop 1
	v_cndmask_b32_e32 v208, 0, v208, vcc
	v_fma_mixlo_f16 v209, v201, s51, 0
	v_add_u32_e32 v167, 5, v166
	v_cmp_gt_u32_e32 vcc, 11, v167
	s_nop 1
	v_cndmask_b32_e32 v209, 0, v209, vcc
	v_fma_mixlo_f16 v210, v202, s51, 0
	v_add_u32_e32 v167, 6, v166
	v_cmp_gt_u32_e32 vcc, 11, v167
	s_nop 1
	v_cndmask_b32_e32 v210, 0, v210, vcc
	v_fma_mixlo_f16 v211, v203, s51, 0
	v_add_u32_e32 v167, 7, v166
	v_cmp_gt_u32_e32 vcc, 11, v167
	s_nop 1
	v_cndmask_b32_e32 v211, 0, v211, vcc
	v_pack_b32_f16 v167, v204, v205
	v_cndmask_b32_e64 v28, 0, v167, s[32:33]
	v_cndmask_b32_e64 v32, 0, v167, s[34:35]
	v_pack_b32_f16 v167, v206, v207
	v_cndmask_b32_e64 v29, 0, v167, s[32:33]
	v_cndmask_b32_e64 v33, 0, v167, s[34:35]
	v_pack_b32_f16 v167, v208, v209
	v_cndmask_b32_e64 v30, 0, v167, s[32:33]
	v_cndmask_b32_e64 v34, 0, v167, s[34:35]
	v_pack_b32_f16 v167, v210, v211
	v_cndmask_b32_e64 v31, 0, v167, s[32:33]
	v_cndmask_b32_e64 v35, 0, v167, s[34:35]
	s_waitcnt lgkmcnt(0)
	s_barrier
	s_cmp_lt_u32 s12, 4
	s_cbranch_scc1 .Lq_noprio
	s_setprio 1
.Lq_noprio:
	s_waitcnt vmcnt(28)
	v_cvt_pk_f16_f32 v164, v36, v40
	v_cvt_pk_f16_f32 v180, v68, v72
	v_pk_add_f16 v164, v164, -0.5 op_sel_hi:[1,0]
	v_pk_add_f16 v180, v180, -0.5 op_sel_hi:[1,0]
	v_pk_mul_f16 v196, v180, v180
	v_pk_mul_f16 v212, v164, v180
	v_pk_fma_f16 v196, v164, v164, v196
	v_cvt_pk_f16_f32 v168, v37, v41
	v_cvt_pk_f16_f32 v184, v69, v73
	v_pk_add_f16 v168, v168, -0.5 op_sel_hi:[1,0]
	v_pk_add_f16 v184, v184, -0.5 op_sel_hi:[1,0]
	v_pk_mul_f16 v200, v184, v184
	v_pk_mul_f16 v216, v168, v184
	v_pk_fma_f16 v200, v168, v168, v200
	v_cvt_pk_f16_f32 v172, v38, v42
	v_cvt_pk_f16_f32 v188, v70, v74
	v_pk_add_f16 v172, v172, -0.5 op_sel_hi:[1,0]
	v_pk_add_f16 v188, v188, -0.5 op_sel_hi:[1,0]
	v_pk_mul_f16 v204, v188, v188
	v_pk_mul_f16 v220, v172, v188
	v_pk_fma_f16 v204, v172, v172, v204
	v_cvt_pk_f16_f32 v176, v39, v43
	v_cvt_pk_f16_f32 v192, v71, v75
	v_pk_add_f16 v176, v176, -0.5 op_sel_hi:[1,0]
	v_pk_add_f16 v192, v192, -0.5 op_sel_hi:[1,0]
	v_pk_mul_f16 v208, v192, v192
	v_pk_mul_f16 v224, v176, v192
	v_pk_fma_f16 v208, v176, v176, v208
	s_waitcnt vmcnt(24)
	v_cvt_pk_f16_f32 v165, v44, v48
	v_cvt_pk_f16_f32 v181, v76, v80
	v_pk_add_f16 v165, v165, -0.5 op_sel_hi:[1,0]
	v_pk_add_f16 v181, v181, -0.5 op_sel_hi:[1,0]
	v_pk_mul_f16 v197, v181, v181
	v_pk_mul_f16 v213, v165, v181
	v_pk_fma_f16 v197, v165, v165, v197
	v_cvt_pk_f16_f32 v169, v45, v49
	v_cvt_pk_f16_f32 v185, v77, v81
	v_pk_add_f16 v169, v169, -0.5 op_sel_hi:[1,0]
	v_pk_add_f16 v185, v185, -0.5 op_sel_hi:[1,0]
	v_pk_mul_f16 v201, v185, v185
	v_pk_mul_f16 v217, v169, v185
	v_pk_fma_f16 v201, v169, v169, v201
	v_cvt_pk_f16_f32 v173, v46, v50
	v_cvt_pk_f16_f32 v189, v78, v82
	v_pk_add_f16 v173, v173, -0.5 op_sel_hi:[1,0]
	v_pk_add_f16 v189, v189, -0.5 op_sel_hi:[1,0]
	v_pk_mul_f16 v205, v189, v189
	v_pk_mul_f16 v221, v173, v189
	v_pk_fma_f16 v205, v173, v173, v205
	v_cvt_pk_f16_f32 v177, v47, v51
	v_cvt_pk_f16_f32 v193, v79, v83
	v_pk_add_f16 v177, v177, -0.5 op_sel_hi:[1,0]
	v_pk_add_f16 v193, v193, -0.5 op_sel_hi:[1,0]
	v_pk_mul_f16 v209, v193, v193
	v_pk_mul_f16 v225, v177, v193
	v_pk_fma_f16 v209, v177, v177, v209
	s_waitcnt vmcnt(20)
	v_cvt_pk_f16_f32 v166, v52, v56
	v_cvt_pk_f16_f32 v182, v84, v88
	v_pk_add_f16 v166, v166, -0.5 op_sel_hi:[1,0]
	v_pk_add_f16 v182, v182, -0.5 op_sel_hi:[1,0]
	v_pk_mul_f16 v198, v182, v182
	v_pk_mul_f16 v214, v166, v182
	v_pk_fma_f16 v198, v166, v166, v198
	v_cvt_pk_f16_f32 v170, v53, v57
	v_cvt_pk_f16_f32 v186, v85, v89
	v_pk_add_f16 v170, v170, -0.5 op_sel_hi:[1,0]
	v_pk_add_f16 v186, v186, -0.5 op_sel_hi:[1,0]
	v_pk_mul_f16 v202, v186, v186
	v_pk_mul_f16 v218, v170, v186
	v_pk_fma_f16 v202, v170, v170, v202
	v_cvt_pk_f16_f32 v174, v54, v58
	v_cvt_pk_f16_f32 v190, v86, v90
	v_pk_add_f16 v174, v174, -0.5 op_sel_hi:[1,0]
	v_pk_add_f16 v190, v190, -0.5 op_sel_hi:[1,0]
	v_pk_mul_f16 v206, v190, v190
	v_pk_mul_f16 v222, v174, v190
	v_pk_fma_f16 v206, v174, v174, v206
	v_cvt_pk_f16_f32 v178, v55, v59
	v_cvt_pk_f16_f32 v194, v87, v91
	v_pk_add_f16 v178, v178, -0.5 op_sel_hi:[1,0]
	v_pk_add_f16 v194, v194, -0.5 op_sel_hi:[1,0]
	v_pk_mul_f16 v210, v194, v194
	v_pk_mul_f16 v226, v178, v194
	v_pk_fma_f16 v210, v178, v178, v210
	s_waitcnt vmcnt(16)
	v_cvt_pk_f16_f32 v167, v60, v64
	v_cvt_pk_f16_f32 v183, v92, v96
	v_pk_add_f16 v167, v167, -0.5 op_sel_hi:[1,0]
	v_pk_add_f16 v183, v183, -0.5 op_sel_hi:[1,0]
	v_pk_mul_f16 v199, v183, v183
	v_pk_mul_f16 v215, v167, v183
	v_pk_fma_f16 v199, v167, v167, v199
	v_cvt_pk_f16_f32 v171, v61, v65
	v_cvt_pk_f16_f32 v187, v93, v97
	v_pk_add_f16 v171, v171, -0.5 op_sel_hi:[1,0]
	v_pk_add_f16 v187, v187, -0.5 op_sel_hi:[1,0]
	v_pk_mul_f16 v203, v187, v187
	v_pk_mul_f16 v219, v171, v187
	v_pk_fma_f16 v203, v171, v171, v203
	v_cvt_pk_f16_f32 v175, v62, v66
	v_cvt_pk_f16_f32 v191, v94, v98
	v_pk_add_f16 v175, v175, -0.5 op_sel_hi:[1,0]
	v_pk_add_f16 v191, v191, -0.5 op_sel_hi:[1,0]
	v_pk_mul_f16 v207, v191, v191
	v_pk_mul_f16 v223, v175, v191
	v_pk_fma_f16 v207, v175, v175, v207
	v_cvt_pk_f16_f32 v179, v63, v67
	v_cvt_pk_f16_f32 v195, v95, v99
	v_pk_add_f16 v179, v179, -0.5 op_sel_hi:[1,0]
	v_pk_add_f16 v195, v195, -0.5 op_sel_hi:[1,0]
	v_pk_mul_f16 v211, v195, v195
	v_pk_mul_f16 v227, v179, v195
	v_pk_fma_f16 v211, v179, v179, v211
	v_mfma_f32_16x16x32_f16 v[68:71], v[164:167], v[24:27], 0
	v_mfma_f32_16x16x32_f16 v[72:75], v[168:171], v[24:27], 0
	v_mfma_f32_16x16x32_f16 v[76:79], v[172:175], v[24:27], 0
	v_mfma_f32_16x16x32_f16 v[80:83], v[176:179], v[24:27], 0
	v_mfma_f32_16x16x32_f16 v[84:87], v[180:183], v[24:27], 0
	v_mfma_f32_16x16x32_f16 v[88:91], v[184:187], v[24:27], 0
	v_mfma_f32_16x16x32_f16 v[92:95], v[188:191], v[24:27], 0
	v_mfma_f32_16x16x32_f16 v[96:99], v[192:195], v[24:27], 0
	s_nop 1
	v_cvt_pk_f16_f32 v36, v68, v72
	s_nop 0
	v_cvt_pk_f16_f32 v37, v76, v80
	v_cvt_pk_f16_f32 v38, v69, v73
	v_cvt_pk_f16_f32 v39, v77, v81
	v_cvt_pk_f16_f32 v40, v70, v74
	v_cvt_pk_f16_f32 v41, v78, v82
	v_cvt_pk_f16_f32 v42, v71, v75
	v_cvt_pk_f16_f32 v43, v79, v83
	v_mfma_f32_16x16x32_f16 v[68:71], v[196:199], v[24:27], 0
	v_mfma_f32_16x16x32_f16 v[72:75], v[200:203], v[24:27], 0
	v_mfma_f32_16x16x32_f16 v[76:79], v[204:207], v[24:27], 0
	v_mfma_f32_16x16x32_f16 v[80:83], v[208:211], v[24:27], 0
	v_cvt_pk_f16_f32 v44, v84, v88
	v_cvt_pk_f16_f32 v45, v92, v96
	v_cvt_pk_f16_f32 v46, v85, v89
	v_cvt_pk_f16_f32 v47, v93, v97
	v_cvt_pk_f16_f32 v48, v86, v90
	v_cvt_pk_f16_f32 v49, v94, v98
	v_cvt_pk_f16_f32 v50, v87, v91
	v_cvt_pk_f16_f32 v51, v95, v99
	v_mfma_f32_16x16x32_f16 v[84:87], v[212:215], v[24:27], 0
	v_mfma_f32_16x16x32_f16 v[88:91], v[216:219], v[24:27], 0
	v_mfma_f32_16x16x32_f16 v[92:95], v[220:223], v[24:27], 0
	v_mfma_f32_16x16x32_f16 v[96:99], v[224:227], v[24:27], 0
	v_cvt_pk_f16_f32 v52, v68, v72
	v_cvt_pk_f16_f32 v53, v76, v80
	v_cvt_pk_f16_f32 v54, v69, v73
	v_cvt_pk_f16_f32 v55, v77, v81
	v_cvt_pk_f16_f32 v56, v70, v74
	v_cvt_pk_f16_f32 v57, v78, v82
	v_cvt_pk_f16_f32 v58, v71, v75
	v_cvt_pk_f16_f32 v59, v79, v83
	v_cvt_pk_f16_f32 v60, v84, v88
	v_cvt_pk_f16_f32 v61, v92, v96
	v_cvt_pk_f16_f32 v62, v85, v89
	v_cvt_pk_f16_f32 v63, v93, v97
	v_cvt_pk_f16_f32 v64, v86, v90
	v_cvt_pk_f16_f32 v65, v94, v98
	v_cvt_pk_f16_f32 v66, v87, v91
	v_cvt_pk_f16_f32 v67, v95, v99
	s_mov_b64 exec, s[38:39]
	ds_write_b128 v4, v[40:43] offset:0
	ds_write_b128 v4, v[48:51] offset:512
	ds_write_b128 v4, v[56:59] offset:1024
	ds_write_b128 v4, v[64:67] offset:1536
	s_mov_b64 exec, -1
	v_mfma_f32_16x16x32_f16 v[68:71], v[24:27], v[36:39], 0
	v_mfma_f32_16x16x32_f16 v[72:75], v[24:27], v[44:47], 0
	v_mfma_f32_16x16x32_f16 v[76:79], v[24:27], v[52:55], v[0:3]
	v_mfma_f32_16x16x32_f16 v[80:83], v[24:27], v[60:63], 0
	v_mfma_f32_16x16x32_f16 v[84:87], v[28:31], v[36:39], 0
	v_mfma_f32_16x16x32_f16 v[88:91], v[28:31], v[44:47], 0
	v_mfma_f32_16x16x32_f16 v[92:95], v[28:31], v[52:55], v[0:3]
	v_mfma_f32_16x16x32_f16 v[96:99], v[28:31], v[60:63], 0
	v_mfma_f32_16x16x32_f16 v[84:87], v[32:35], v[40:43], v[84:87]
	v_mfma_f32_16x16x32_f16 v[88:91], v[32:35], v[48:51], v[88:91]
	v_mfma_f32_16x16x32_f16 v[92:95], v[32:35], v[56:59], v[92:95]
	v_mfma_f32_16x16x32_f16 v[96:99], v[32:35], v[64:67], v[96:99]
	s_waitcnt lgkmcnt(0)
	ds_write_b32 v6, v6 offset:0
	ds_read_b32 v9, v7 offset:0
	v_mul_f32_e32 v244, v68, v72
	v_mul_f32_e32 v250, v69, v73
	v_mul_f32_e64 v245, -v72, v72
	v_mul_f32_e64 v251, -v73, v73
	v_add_f32_e32 v246, v68, v72
	v_add_f32_e32 v252, v69, v73
	v_fma_f32 v245, -v68, v68, v245
	v_fma_f32 v251, -v69, v69, v251
	v_fma_f32 v247, v10, v246, v11
	v_fma_f32 v253, v10, v252, v11
	v_fma_f32 v246, v13, v80, v14
	v_fma_f32 v252, v13, v81, v14
	v_fma_f32 v248, v12, v76, v245
	v_fma_f32 v254, v12, v77, v251
	v_fma_f32 v249, 2.0, v244, v247
	v_fma_f32 v255, 2.0, v250, v253
	v_sub_f32_e32 v247, v247, v245
	v_sub_f32_e32 v253, v253, v251
	v_fma_f32 v246, -2.0, v244, v246
	v_fma_f32 v252, -2.0, v250, v252
	v_mul_f32_e32 v247, v247, v248
	v_mul_f32_e32 v253, v253, v254
	v_rcp_f32_e32 v247, v247
	v_rcp_f32_e32 v253, v253
	v_mul_f32_e32 v249, v249, v246
	v_mul_f32_e32 v255, v255, v252
	v_fma_f32 v19, v249, v247, v19
	v_fma_f32 v19, v255, v253, v19
	v_mul_f32_e32 v244, v70, v74
	v_mul_f32_e32 v250, v71, v75
	v_mul_f32_e64 v245, -v74, v74
	v_mul_f32_e64 v251, -v75, v75
	v_add_f32_e32 v246, v70, v74
	v_add_f32_e32 v252, v71, v75
	v_fma_f32 v245, -v70, v70, v245
	v_fma_f32 v251, -v71, v71, v251
	v_fma_f32 v247, v10, v246, v11
	v_fma_f32 v253, v10, v252, v11
	v_fma_f32 v246, v13, v82, v14
	v_fma_f32 v252, v13, v83, v14
	v_fma_f32 v248, v12, v78, v245
	v_fma_f32 v254, v12, v79, v251
	v_fma_f32 v249, 2.0, v244, v247
	v_fma_f32 v255, 2.0, v250, v253
	v_sub_f32_e32 v247, v247, v245
	v_sub_f32_e32 v253, v253, v251
	v_fma_f32 v246, -2.0, v244, v246
	v_fma_f32 v252, -2.0, v250, v252
	v_mul_f32_e32 v247, v247, v248
	v_mul_f32_e32 v253, v253, v254
	v_rcp_f32_e32 v247, v247
	v_rcp_f32_e32 v253, v253
	v_mul_f32_e32 v249, v249, v246
	v_mul_f32_e32 v255, v255, v252
	v_fma_f32 v20, v249, v247, v20
	v_fma_f32 v20, v255, v253, v20
	v_mfma_f32_16x16x32_f16 v[68:71], v[24:27], v[40:43], 0
	v_mfma_f32_16x16x32_f16 v[72:75], v[24:27], v[48:51], 0
	v_mfma_f32_16x16x32_f16 v[76:79], v[24:27], v[56:59], v[0:3]
	v_mfma_f32_16x16x32_f16 v[80:83], v[24:27], v[64:67], 0
	s_waitcnt lgkmcnt(0)
	v_cmp_ne_u32_e32 vcc, 0, v9
	s_cbranch_vccnz .Lq_go_0
